# PEER combine phase rewritten by hand: 32 independent loads of a step issued together + 16 dependent gathers (was 5 serial waits per step)
# speedup vs baseline: 1.0046x; 1.0046x over previous
.LBB0_1117:
	s_andn2_b64 vcc, exec, s[6:7]
	s_cbranch_vccnz .LBB0_1177
	v_readfirstlane_b32 s14, v0
	s_and_b32 s14, s14, 0xffffffc0
	s_lshl_b32 s6, s2, 9
	s_add_u32 s6, s6, s14
	s_lshl_b32 s7, s96, 4
	s_cmp_ge_u32 s6, s7
	s_cbranch_scc1 .Lcmb_end
	s_lshl_b32 s12, s82, 9
	v_readlane_b32 s4, v252, 4
	v_readlane_b32 s5, v252, 5
	v_readlane_b32 s15, v255, 34
	s_sub_u32 s4, s4, 0x18
	s_subb_u32 s5, s5, 0
	s_load_dwordx2 s[4:5], s[4:5], 0x0
	s_lshl_b32 s15, s15, 16
	s_mov_b32 s13, 0x3e6d3389
	v_and_b32_e32 v2, 63, v0
	v_and_b32_e32 v3, 15, v2
	v_cmp_eq_u32_e64 s[38:39], 0, v3
	v_lshrrev_b32_e32 v146, 2, v3
	v_and_b32_e32 v147, 1, v3
	v_lshl_add_u32 v146, v147, 2, v146
	v_bfe_u32 v147, v3, 1, 1
	v_lshl_add_u32 v89, v146, 4, v147
	s_waitcnt lgkmcnt(0)
	s_add_u32 s8, s4, s15
	s_addc_u32 s9, s5, 0
	s_add_u32 s10, s8, 0x12a20000
	s_addc_u32 s11, s9, 0
	s_add_u32 s8, s8, 0x12a00000
	s_addc_u32 s9, s9, 0
.Lcmb_loop:
	v_add_u32_e32 v5, s6, v2
	v_lshrrev_b32_e32 v146, 4, v5
	v_lshl_add_u32 v147, v146, 7, v89
	v_lshlrev_b32_e32 v148, 2, v147
	v_add_u32_e32 v86, 0x2e400000, v148
	v_add_u32_e32 v87, 0x2f000000, v148
	v_add_u32_e32 v88, 0x39c00000, v147
	v_lshlrev_b32_e32 v148, 4, v5
	v_add_u32_e32 v70, 0x30000000, v148
	v_add_u32_e32 v71, 0x440000, v70
	v_add_u32_e32 v72, 0x880000, v70
	v_add_u32_e32 v73, 0xcc0000, v70
	v_add_u32_e32 v74, 0x1100000, v70
	v_add_u32_e32 v75, 0x1540000, v70
	v_add_u32_e32 v76, 0x1980000, v70
	v_add_u32_e32 v77, 0x1dc0000, v70
	v_add_u32_e32 v78, 0x2200000, v70
	v_add_u32_e32 v79, 0x2640000, v70
	v_add_u32_e32 v80, 0x2a80000, v70
	v_add_u32_e32 v81, 0x2ec0000, v70
	v_add_u32_e32 v82, 0x3300000, v70
	v_add_u32_e32 v83, 0x3740000, v70
	v_add_u32_e32 v84, 0x3b80000, v70
	v_add_u32_e32 v85, 0x3fc0000, v70
	global_load_dwordx4 v[6:9], v70, s[4:5] nt
	global_load_dwordx4 v[10:13], v71, s[4:5] nt
	global_load_dwordx4 v[14:17], v72, s[4:5] nt
	global_load_dwordx4 v[18:21], v73, s[4:5] nt
	global_load_dwordx4 v[22:25], v74, s[4:5] nt
	global_load_dwordx4 v[26:29], v75, s[4:5] nt
	global_load_dwordx4 v[30:33], v76, s[4:5] nt
	global_load_dwordx4 v[34:37], v77, s[4:5] nt
	global_load_dwordx4 v[38:41], v78, s[4:5] nt
	global_load_dwordx4 v[42:45], v79, s[4:5] nt
	global_load_dwordx4 v[46:49], v80, s[4:5] nt
	global_load_dwordx4 v[50:53], v81, s[4:5] nt
	global_load_dwordx4 v[54:57], v82, s[4:5] nt
	global_load_dwordx4 v[58:61], v83, s[4:5] nt
	global_load_dwordx4 v[62:65], v84, s[4:5] nt
	global_load_dwordx4 v[66:69], v85, s[4:5] nt
	global_load_dword v90, v86, s[4:5]
	global_load_dword v91, v86, s[4:5] offset:8
	global_load_dword v92, v86, s[4:5] offset:16
	global_load_dword v93, v86, s[4:5] offset:24
	global_load_dword v94, v86, s[4:5] offset:32
	global_load_dword v95, v86, s[4:5] offset:40
	global_load_dword v96, v86, s[4:5] offset:48
	global_load_dword v97, v86, s[4:5] offset:56
	global_load_dword v98, v87, s[4:5]
	global_load_dword v99, v87, s[4:5] offset:8
	global_load_dword v100, v87, s[4:5] offset:16
	global_load_dword v101, v87, s[4:5] offset:24
	global_load_dword v102, v87, s[4:5] offset:32
	global_load_dword v103, v87, s[4:5] offset:40
	global_load_dword v104, v87, s[4:5] offset:48
	global_load_dword v105, v87, s[4:5] offset:56
	s_waitcnt vmcnt(8)
	v_lshlrev_b32_e32 v122, 2, v90
	v_lshlrev_b32_e32 v123, 2, v91
	v_lshlrev_b32_e32 v124, 2, v92
	v_lshlrev_b32_e32 v125, 2, v93
	v_lshlrev_b32_e32 v126, 2, v94
	v_lshlrev_b32_e32 v127, 2, v95
	v_lshlrev_b32_e32 v128, 2, v96
	v_lshlrev_b32_e32 v129, 2, v97
	global_load_dword v106, v122, s[8:9]
	global_load_dword v107, v123, s[8:9]
	global_load_dword v108, v124, s[8:9]
	global_load_dword v109, v125, s[8:9]
	global_load_dword v110, v126, s[8:9]
	global_load_dword v111, v127, s[8:9]
	global_load_dword v112, v128, s[8:9]
	global_load_dword v113, v129, s[8:9]
	global_load_dword v114, v122, s[10:11]
	global_load_dword v115, v123, s[10:11]
	global_load_dword v116, v124, s[10:11]
	global_load_dword v117, v125, s[10:11]
	global_load_dword v118, v126, s[10:11]
	global_load_dword v119, v127, s[10:11]
	global_load_dword v120, v128, s[10:11]
	global_load_dword v121, v129, s[10:11]
	v_lshlrev_b32_e32 v130, 16, v6
	v_and_b32_e32 v131, 0xffff0000, v6
	v_lshlrev_b32_e32 v132, 16, v7
	v_and_b32_e32 v133, 0xffff0000, v7
	v_lshlrev_b32_e32 v134, 16, v8
	v_and_b32_e32 v135, 0xffff0000, v8
	v_lshlrev_b32_e32 v136, 16, v9
	v_and_b32_e32 v137, 0xffff0000, v9
	v_lshlrev_b32_e32 v146, 16, v10
	v_and_b32_e32 v147, 0xffff0000, v10
	v_lshlrev_b32_e32 v148, 16, v11
	v_and_b32_e32 v149, 0xffff0000, v11
	v_lshlrev_b32_e32 v150, 16, v12
	v_and_b32_e32 v151, 0xffff0000, v12
	v_lshlrev_b32_e32 v152, 16, v13
	v_and_b32_e32 v153, 0xffff0000, v13
	v_pk_add_f32 v[130:131], v[130:131], v[146:147]
	v_pk_add_f32 v[132:133], v[132:133], v[148:149]
	v_pk_add_f32 v[134:135], v[134:135], v[150:151]
	v_pk_add_f32 v[136:137], v[136:137], v[152:153]
	v_lshlrev_b32_e32 v146, 16, v14
	v_and_b32_e32 v147, 0xffff0000, v14
	v_lshlrev_b32_e32 v148, 16, v15
	v_and_b32_e32 v149, 0xffff0000, v15
	v_lshlrev_b32_e32 v150, 16, v16
	v_and_b32_e32 v151, 0xffff0000, v16
	v_lshlrev_b32_e32 v152, 16, v17
	v_and_b32_e32 v153, 0xffff0000, v17
	v_pk_add_f32 v[130:131], v[130:131], v[146:147]
	v_pk_add_f32 v[132:133], v[132:133], v[148:149]
	v_pk_add_f32 v[134:135], v[134:135], v[150:151]
	v_pk_add_f32 v[136:137], v[136:137], v[152:153]
	v_lshlrev_b32_e32 v146, 16, v18
	v_and_b32_e32 v147, 0xffff0000, v18
	v_lshlrev_b32_e32 v148, 16, v19
	v_and_b32_e32 v149, 0xffff0000, v19
	v_lshlrev_b32_e32 v150, 16, v20
	v_and_b32_e32 v151, 0xffff0000, v20
	v_lshlrev_b32_e32 v152, 16, v21
	v_and_b32_e32 v153, 0xffff0000, v21
	v_pk_add_f32 v[130:131], v[130:131], v[146:147]
	v_pk_add_f32 v[132:133], v[132:133], v[148:149]
	v_pk_add_f32 v[134:135], v[134:135], v[150:151]
	v_pk_add_f32 v[136:137], v[136:137], v[152:153]
	v_lshlrev_b32_e32 v146, 16, v22
	v_and_b32_e32 v147, 0xffff0000, v22
	v_lshlrev_b32_e32 v148, 16, v23
	v_and_b32_e32 v149, 0xffff0000, v23
	v_lshlrev_b32_e32 v150, 16, v24
	v_and_b32_e32 v151, 0xffff0000, v24
	v_lshlrev_b32_e32 v152, 16, v25
	v_and_b32_e32 v153, 0xffff0000, v25
	v_pk_add_f32 v[130:131], v[130:131], v[146:147]
	v_pk_add_f32 v[132:133], v[132:133], v[148:149]
	v_pk_add_f32 v[134:135], v[134:135], v[150:151]
	v_pk_add_f32 v[136:137], v[136:137], v[152:153]
	v_lshlrev_b32_e32 v146, 16, v26
	v_and_b32_e32 v147, 0xffff0000, v26
	v_lshlrev_b32_e32 v148, 16, v27
	v_and_b32_e32 v149, 0xffff0000, v27
	v_lshlrev_b32_e32 v150, 16, v28
	v_and_b32_e32 v151, 0xffff0000, v28
	v_lshlrev_b32_e32 v152, 16, v29
	v_and_b32_e32 v153, 0xffff0000, v29
	v_pk_add_f32 v[130:131], v[130:131], v[146:147]
	v_pk_add_f32 v[132:133], v[132:133], v[148:149]
	v_pk_add_f32 v[134:135], v[134:135], v[150:151]
	v_pk_add_f32 v[136:137], v[136:137], v[152:153]
	v_lshlrev_b32_e32 v146, 16, v30
	v_and_b32_e32 v147, 0xffff0000, v30
	v_lshlrev_b32_e32 v148, 16, v31
	v_and_b32_e32 v149, 0xffff0000, v31
	v_lshlrev_b32_e32 v150, 16, v32
	v_and_b32_e32 v151, 0xffff0000, v32
	v_lshlrev_b32_e32 v152, 16, v33
	v_and_b32_e32 v153, 0xffff0000, v33
	v_pk_add_f32 v[130:131], v[130:131], v[146:147]
	v_pk_add_f32 v[132:133], v[132:133], v[148:149]
	v_pk_add_f32 v[134:135], v[134:135], v[150:151]
	v_pk_add_f32 v[136:137], v[136:137], v[152:153]
	v_lshlrev_b32_e32 v146, 16, v34
	v_and_b32_e32 v147, 0xffff0000, v34
	v_lshlrev_b32_e32 v148, 16, v35
	v_and_b32_e32 v149, 0xffff0000, v35
	v_lshlrev_b32_e32 v150, 16, v36
	v_and_b32_e32 v151, 0xffff0000, v36
	v_lshlrev_b32_e32 v152, 16, v37
	v_and_b32_e32 v153, 0xffff0000, v37
	v_pk_add_f32 v[130:131], v[130:131], v[146:147]
	v_pk_add_f32 v[132:133], v[132:133], v[148:149]
	v_pk_add_f32 v[134:135], v[134:135], v[150:151]
	v_pk_add_f32 v[136:137], v[136:137], v[152:153]
	v_lshlrev_b32_e32 v146, 16, v38
	v_and_b32_e32 v147, 0xffff0000, v38
	v_lshlrev_b32_e32 v148, 16, v39
	v_and_b32_e32 v149, 0xffff0000, v39
	v_lshlrev_b32_e32 v150, 16, v40
	v_and_b32_e32 v151, 0xffff0000, v40
	v_lshlrev_b32_e32 v152, 16, v41
	v_and_b32_e32 v153, 0xffff0000, v41
	v_pk_add_f32 v[130:131], v[130:131], v[146:147]
	v_pk_add_f32 v[132:133], v[132:133], v[148:149]
	v_pk_add_f32 v[134:135], v[134:135], v[150:151]
	v_pk_add_f32 v[136:137], v[136:137], v[152:153]
	v_lshlrev_b32_e32 v146, 16, v42
	v_and_b32_e32 v147, 0xffff0000, v42
	v_lshlrev_b32_e32 v148, 16, v43
	v_and_b32_e32 v149, 0xffff0000, v43
	v_lshlrev_b32_e32 v150, 16, v44
	v_and_b32_e32 v151, 0xffff0000, v44
	v_lshlrev_b32_e32 v152, 16, v45
	v_and_b32_e32 v153, 0xffff0000, v45
	v_pk_add_f32 v[130:131], v[130:131], v[146:147]
	v_pk_add_f32 v[132:133], v[132:133], v[148:149]
	v_pk_add_f32 v[134:135], v[134:135], v[150:151]
	v_pk_add_f32 v[136:137], v[136:137], v[152:153]
	v_lshlrev_b32_e32 v146, 16, v46
	v_and_b32_e32 v147, 0xffff0000, v46
	v_lshlrev_b32_e32 v148, 16, v47
	v_and_b32_e32 v149, 0xffff0000, v47
	v_lshlrev_b32_e32 v150, 16, v48
	v_and_b32_e32 v151, 0xffff0000, v48
	v_lshlrev_b32_e32 v152, 16, v49
	v_and_b32_e32 v153, 0xffff0000, v49
	v_pk_add_f32 v[130:131], v[130:131], v[146:147]
	v_pk_add_f32 v[132:133], v[132:133], v[148:149]
	v_pk_add_f32 v[134:135], v[134:135], v[150:151]
	v_pk_add_f32 v[136:137], v[136:137], v[152:153]
	v_lshlrev_b32_e32 v146, 16, v50
	v_and_b32_e32 v147, 0xffff0000, v50
	v_lshlrev_b32_e32 v148, 16, v51
	v_and_b32_e32 v149, 0xffff0000, v51
	v_lshlrev_b32_e32 v150, 16, v52
	v_and_b32_e32 v151, 0xffff0000, v52
	v_lshlrev_b32_e32 v152, 16, v53
	v_and_b32_e32 v153, 0xffff0000, v53
	v_pk_add_f32 v[130:131], v[130:131], v[146:147]
	v_pk_add_f32 v[132:133], v[132:133], v[148:149]
	v_pk_add_f32 v[134:135], v[134:135], v[150:151]
	v_pk_add_f32 v[136:137], v[136:137], v[152:153]
	v_lshlrev_b32_e32 v146, 16, v54
	v_and_b32_e32 v147, 0xffff0000, v54
	v_lshlrev_b32_e32 v148, 16, v55
	v_and_b32_e32 v149, 0xffff0000, v55
	v_lshlrev_b32_e32 v150, 16, v56
	v_and_b32_e32 v151, 0xffff0000, v56
	v_lshlrev_b32_e32 v152, 16, v57
	v_and_b32_e32 v153, 0xffff0000, v57
	v_pk_add_f32 v[130:131], v[130:131], v[146:147]
	v_pk_add_f32 v[132:133], v[132:133], v[148:149]
	v_pk_add_f32 v[134:135], v[134:135], v[150:151]
	v_pk_add_f32 v[136:137], v[136:137], v[152:153]
	v_lshlrev_b32_e32 v146, 16, v58
	v_and_b32_e32 v147, 0xffff0000, v58
	v_lshlrev_b32_e32 v148, 16, v59
	v_and_b32_e32 v149, 0xffff0000, v59
	v_lshlrev_b32_e32 v150, 16, v60
	v_and_b32_e32 v151, 0xffff0000, v60
	v_lshlrev_b32_e32 v152, 16, v61
	v_and_b32_e32 v153, 0xffff0000, v61
	v_pk_add_f32 v[130:131], v[130:131], v[146:147]
	v_pk_add_f32 v[132:133], v[132:133], v[148:149]
	v_pk_add_f32 v[134:135], v[134:135], v[150:151]
	v_pk_add_f32 v[136:137], v[136:137], v[152:153]
	v_lshlrev_b32_e32 v146, 16, v62
	v_and_b32_e32 v147, 0xffff0000, v62
	v_lshlrev_b32_e32 v148, 16, v63
	v_and_b32_e32 v149, 0xffff0000, v63
	v_lshlrev_b32_e32 v150, 16, v64
	v_and_b32_e32 v151, 0xffff0000, v64
	v_lshlrev_b32_e32 v152, 16, v65
	v_and_b32_e32 v153, 0xffff0000, v65
	v_pk_add_f32 v[130:131], v[130:131], v[146:147]
	v_pk_add_f32 v[132:133], v[132:133], v[148:149]
	v_pk_add_f32 v[134:135], v[134:135], v[150:151]
	v_pk_add_f32 v[136:137], v[136:137], v[152:153]
	v_lshlrev_b32_e32 v146, 16, v66
	v_and_b32_e32 v147, 0xffff0000, v66
	v_lshlrev_b32_e32 v148, 16, v67
	v_and_b32_e32 v149, 0xffff0000, v67
	v_lshlrev_b32_e32 v150, 16, v68
	v_and_b32_e32 v151, 0xffff0000, v68
	v_lshlrev_b32_e32 v152, 16, v69
	v_and_b32_e32 v153, 0xffff0000, v69
	v_pk_add_f32 v[130:131], v[130:131], v[146:147]
	v_pk_add_f32 v[132:133], v[132:133], v[148:149]
	v_pk_add_f32 v[134:135], v[134:135], v[150:151]
	v_pk_add_f32 v[136:137], v[136:137], v[152:153]
	s_waitcnt vmcnt(0)
	v_mul_f32_e32 v146, v130, v106
	v_mul_f32_e32 v147, v131, v107
	v_fma_f32 v148, |v146|, s13, 1.0
	v_fma_f32 v149, |v147|, s13, 1.0
	v_rcp_f32_e32 v148, v148
	v_rcp_f32_e32 v149, v149
	v_mul_f32_e32 v152, v146, v146
	v_mul_f32_e32 v153, v147, v147
	v_fmamk_f32 v150, v148, 0x3f07dc22, v207
	v_fmamk_f32 v151, v149, 0x3f07dc22, v207
	v_fmaak_f32 v150, v148, v150, 0x3f35f0e3
	v_fmaak_f32 v151, v149, v151, 0x3f35f0e3
	v_fmaak_f32 v150, v148, v150, 0xbe11a98e
	v_fmaak_f32 v151, v149, v151, 0xbe11a98e
	v_fmaak_f32 v150, v148, v150, 0x3e027906
	v_fmaak_f32 v151, v149, v151, 0x3e027906
	v_mul_f32_e32 v150, v148, v150
	v_mul_f32_e32 v151, v149, v151
	v_mul_f32_e32 v152, 0xbf38aa3b, v152
	v_mul_f32_e32 v153, 0xbf38aa3b, v153
	v_exp_f32_e32 v152, v152
	v_exp_f32_e32 v153, v153
	v_cmp_gt_f32_e64 s[40:41], 0, v146
	v_cmp_gt_f32_e32 vcc, 0, v147
	v_mul_f32_e32 v150, v152, v150
	v_mul_f32_e32 v151, v153, v151
	v_mul_f32_e32 v148, v146, v150
	v_mul_f32_e32 v149, v147, v151
	v_fma_f32 v150, -v146, v150, v146
	v_fma_f32 v151, -v147, v151, v147
	v_cndmask_b32_e64 v150, v150, v148, s[40:41]
	v_cndmask_b32_e32 v151, v151, v149, vcc
	v_mul_f32_e32 v138, v98, v150
	v_mul_f32_e32 v139, v99, v151
	v_mul_f32_e32 v138, v114, v138
	v_mul_f32_e32 v139, v115, v139
	v_mul_f32_e32 v146, v132, v108
	v_mul_f32_e32 v147, v133, v109
	v_fma_f32 v148, |v146|, s13, 1.0
	v_fma_f32 v149, |v147|, s13, 1.0
	v_rcp_f32_e32 v148, v148
	v_rcp_f32_e32 v149, v149
	v_mul_f32_e32 v152, v146, v146
	v_mul_f32_e32 v153, v147, v147
	v_fmamk_f32 v150, v148, 0x3f07dc22, v207
	v_fmamk_f32 v151, v149, 0x3f07dc22, v207
	v_fmaak_f32 v150, v148, v150, 0x3f35f0e3
	v_fmaak_f32 v151, v149, v151, 0x3f35f0e3
	v_fmaak_f32 v150, v148, v150, 0xbe11a98e
	v_fmaak_f32 v151, v149, v151, 0xbe11a98e
	v_fmaak_f32 v150, v148, v150, 0x3e027906
	v_fmaak_f32 v151, v149, v151, 0x3e027906
	v_mul_f32_e32 v150, v148, v150
	v_mul_f32_e32 v151, v149, v151
	v_mul_f32_e32 v152, 0xbf38aa3b, v152
	v_mul_f32_e32 v153, 0xbf38aa3b, v153
	v_exp_f32_e32 v152, v152
	v_exp_f32_e32 v153, v153
	v_cmp_gt_f32_e64 s[40:41], 0, v146
	v_cmp_gt_f32_e32 vcc, 0, v147
	v_mul_f32_e32 v150, v152, v150
	v_mul_f32_e32 v151, v153, v151
	v_mul_f32_e32 v148, v146, v150
	v_mul_f32_e32 v149, v147, v151
	v_fma_f32 v150, -v146, v150, v146
	v_fma_f32 v151, -v147, v151, v147
	v_cndmask_b32_e64 v150, v150, v148, s[40:41]
	v_cndmask_b32_e32 v151, v151, v149, vcc
	v_mul_f32_e32 v140, v100, v150
	v_mul_f32_e32 v141, v101, v151
	v_mul_f32_e32 v140, v116, v140
	v_mul_f32_e32 v141, v117, v141
	v_mul_f32_e32 v146, v134, v110
	v_mul_f32_e32 v147, v135, v111
	v_fma_f32 v148, |v146|, s13, 1.0
	v_fma_f32 v149, |v147|, s13, 1.0
	v_rcp_f32_e32 v148, v148
	v_rcp_f32_e32 v149, v149
	v_mul_f32_e32 v152, v146, v146
	v_mul_f32_e32 v153, v147, v147
	v_fmamk_f32 v150, v148, 0x3f07dc22, v207
	v_fmamk_f32 v151, v149, 0x3f07dc22, v207
	v_fmaak_f32 v150, v148, v150, 0x3f35f0e3
	v_fmaak_f32 v151, v149, v151, 0x3f35f0e3
	v_fmaak_f32 v150, v148, v150, 0xbe11a98e
	v_fmaak_f32 v151, v149, v151, 0xbe11a98e
	v_fmaak_f32 v150, v148, v150, 0x3e027906
	v_fmaak_f32 v151, v149, v151, 0x3e027906
	v_mul_f32_e32 v150, v148, v150
	v_mul_f32_e32 v151, v149, v151
	v_mul_f32_e32 v152, 0xbf38aa3b, v152
	v_mul_f32_e32 v153, 0xbf38aa3b, v153
	v_exp_f32_e32 v152, v152
	v_exp_f32_e32 v153, v153
	v_cmp_gt_f32_e64 s[40:41], 0, v146
	v_cmp_gt_f32_e32 vcc, 0, v147
	v_mul_f32_e32 v150, v152, v150
	v_mul_f32_e32 v151, v153, v151
	v_mul_f32_e32 v148, v146, v150
	v_mul_f32_e32 v149, v147, v151
	v_fma_f32 v150, -v146, v150, v146
	v_fma_f32 v151, -v147, v151, v147
	v_cndmask_b32_e64 v150, v150, v148, s[40:41]
	v_cndmask_b32_e32 v151, v151, v149, vcc
	v_mul_f32_e32 v142, v102, v150
	v_mul_f32_e32 v143, v103, v151
	v_mul_f32_e32 v142, v118, v142
	v_mul_f32_e32 v143, v119, v143
	v_mul_f32_e32 v146, v136, v112
	v_mul_f32_e32 v147, v137, v113
	v_fma_f32 v148, |v146|, s13, 1.0
	v_fma_f32 v149, |v147|, s13, 1.0
	v_rcp_f32_e32 v148, v148
	v_rcp_f32_e32 v149, v149
	v_mul_f32_e32 v152, v146, v146
	v_mul_f32_e32 v153, v147, v147
	v_fmamk_f32 v150, v148, 0x3f07dc22, v207
	v_fmamk_f32 v151, v149, 0x3f07dc22, v207
	v_fmaak_f32 v150, v148, v150, 0x3f35f0e3
	v_fmaak_f32 v151, v149, v151, 0x3f35f0e3
	v_fmaak_f32 v150, v148, v150, 0xbe11a98e
	v_fmaak_f32 v151, v149, v151, 0xbe11a98e
	v_fmaak_f32 v150, v148, v150, 0x3e027906
	v_fmaak_f32 v151, v149, v151, 0x3e027906
	v_mul_f32_e32 v150, v148, v150
	v_mul_f32_e32 v151, v149, v151
	v_mul_f32_e32 v152, 0xbf38aa3b, v152
	v_mul_f32_e32 v153, 0xbf38aa3b, v153
	v_exp_f32_e32 v152, v152
	v_exp_f32_e32 v153, v153
	v_cmp_gt_f32_e64 s[40:41], 0, v146
	v_cmp_gt_f32_e32 vcc, 0, v147
	v_mul_f32_e32 v150, v152, v150
	v_mul_f32_e32 v151, v153, v151
	v_mul_f32_e32 v148, v146, v150
	v_mul_f32_e32 v149, v147, v151
	v_fma_f32 v150, -v146, v150, v146
	v_fma_f32 v151, -v147, v151, v147
	v_cndmask_b32_e64 v150, v150, v148, s[40:41]
	v_cndmask_b32_e32 v151, v151, v149, vcc
	v_mul_f32_e32 v144, v104, v150
	v_mul_f32_e32 v145, v105, v151
	v_mul_f32_e32 v144, v120, v144
	v_mul_f32_e32 v145, v121, v145
	v_max3_f32 v146, |v138|, 0, |v139|
	v_max3_f32 v146, v146, |v140|, |v141|
	v_max3_f32 v146, v146, |v142|, |v143|
	v_max3_f32 v146, v146, |v144|, |v145|
	s_nop 1
	v_mov_b32_dpp v147, v146 quad_perm:[1,0,3,2] row_mask:0xf bank_mask:0xf bound_ctrl:1
	v_max_f32_e32 v147, v147, v147
	v_max_f32_e32 v146, v146, v147
	s_nop 1
	v_mov_b32_dpp v147, v146 quad_perm:[2,3,0,1] row_mask:0xf bank_mask:0xf bound_ctrl:1
	v_max_f32_e32 v147, v147, v147
	v_max_f32_e32 v146, v146, v147
	s_nop 1
	v_mov_b32_dpp v147, v146 row_half_mirror row_mask:0xf bank_mask:0xf bound_ctrl:1
	v_max_f32_e32 v147, v147, v147
	v_max_f32_e32 v146, v146, v147
	s_nop 1
	v_mov_b32_dpp v147, v146 row_mirror row_mask:0xf bank_mask:0xf bound_ctrl:1
	v_max_f32_e32 v147, v147, v147
	v_max_f32_e32 v146, v146, v147
	v_div_scale_f32 v148, s[100:101], v146, v146, s95
	v_rcp_f32_e32 v149, v148
	v_div_scale_f32 v150, vcc, s95, v146, s95
	v_fma_f32 v151, -v148, v149, 1.0
	v_fmac_f32_e32 v149, v151, v149
	v_mul_f32_e32 v151, v150, v149
	v_fma_f32 v152, -v148, v151, v150
	v_fmac_f32_e32 v151, v152, v149
	v_fma_f32 v148, -v148, v151, v150
	v_div_fmas_f32 v148, v148, v149, v151
	v_div_fixup_f32 v148, v148, v146, s95
	v_cmp_lt_f32_e32 vcc, 0, v146
	s_nop 1
	v_cndmask_b32_e32 v149, 0, v148, vcc
	v_mul_f32_e32 v138, v138, v149
	v_mul_f32_e32 v139, v139, v149
	v_mul_f32_e32 v140, v140, v149
	v_mul_f32_e32 v141, v141, v149
	v_mul_f32_e32 v142, v142, v149
	v_mul_f32_e32 v143, v143, v149
	v_mul_f32_e32 v144, v144, v149
	v_mul_f32_e32 v145, v145, v149
	v_med3_f32 v138, v138, s79, v204
	v_med3_f32 v139, v139, s79, v204
	v_med3_f32 v140, v140, s79, v204
	v_med3_f32 v141, v141, s79, v204
	v_med3_f32 v142, v142, s79, v204
	v_med3_f32 v143, v143, s79, v204
	v_med3_f32 v144, v144, s79, v204
	v_med3_f32 v145, v145, s79, v204
	v_mov_b32_e32 v130, v4
	v_mov_b32_e32 v131, v4
	v_mov_b32_e32 v132, v4
	v_mov_b32_e32 v133, v4
	v_mov_b32_e32 v134, v4
	v_mov_b32_e32 v135, v4
	v_mov_b32_e32 v136, v4
	v_mov_b32_e32 v137, v4
	v_cvt_pk_fp8_f32 v130, v138, v138
	v_cvt_pk_fp8_f32 v131, v139, v139
	v_cvt_pk_fp8_f32 v132, v140, v140
	v_cvt_pk_fp8_f32 v133, v141, v141
	v_cvt_pk_fp8_f32 v134, v142, v142
	v_cvt_pk_fp8_f32 v135, v143, v143
	v_cvt_pk_fp8_f32 v136, v144, v144
	v_cvt_pk_fp8_f32 v137, v145, v145
	global_store_byte v88, v130, s[4:5]
	global_store_byte v88, v131, s[4:5] offset:2
	global_store_byte v88, v132, s[4:5] offset:4
	global_store_byte v88, v133, s[4:5] offset:6
	global_store_byte v88, v134, s[4:5] offset:8
	global_store_byte v88, v135, s[4:5] offset:10
	global_store_byte v88, v136, s[4:5] offset:12
	global_store_byte v88, v137, s[4:5] offset:14
	v_mul_f32_e32 v150, 0x3b124925, v146
	v_cndmask_b32_e32 v150, 1.0, v150, vcc
	v_lshrrev_b32_e32 v151, 4, v5
	v_lshlrev_b32_e32 v151, 2, v151
	v_add_u32_e32 v151, 0x39f00000, v151
	s_mov_b64 exec, s[38:39]
	global_store_dword v151, v150, s[4:5]
	s_mov_b64 exec, -1
	s_add_u32 s6, s6, s12
	s_cmp_lt_u32 s6, s7
	s_cbranch_scc1 .Lcmb_loop
.Lcmb_end:
	s_mov_b64 s[6:7], -1
